# router: bias-constant loop issues its four weight loads and bias load together (counted waits) instead of five dependent round trips per group
# speedup vs baseline: 1.0093x; 1.0002x over previous
.LBB0_1207:
	s_ashr_i32 s1, s0, 31
	v_lshl_add_u64 v[22:23], s[0:1], 2, v[58:59]
	global_load_dwordx4 v[124:127], v[22:23], off
	global_load_dwordx4 v[128:131], v[22:23], off offset:1024
	global_load_dwordx4 v[132:135], v[22:23], off offset:2048
	global_load_dwordx4 v[136:139], v[22:23], off offset:3072
	s_lshl_b64 s[34:35], s[80:81], 2
	s_add_u32 s34, s2, s34
	s_addc_u32 s35, s3, s35
	s_add_u32 s34, s34, -16
	s_addc_u32 s35, s35, -1
	s_cmp_lt_i32 s80, 4
	s_cselect_b32 s35, s23, s35
	s_cselect_b32 s34, s22, s34
	s_and_saveexec_b64 s[24:25], s[40:41]
	global_load_dword v140, v115, s[34:35]
	s_or_b64 exec, exec, s[24:25]
	s_waitcnt vmcnt(4)
	v_mul_f32_e32 v19, v125, v11
	v_fmac_f32_e32 v19, v124, v10
	v_fmac_f32_e32 v19, v126, v12
	v_fmac_f32_e32 v19, v127, v13
	v_add_f32_e32 v24, 0, v19
	s_waitcnt vmcnt(3)
	v_mul_f32_e32 v19, v129, v3
	v_fmac_f32_e32 v19, v128, v2
	v_fmac_f32_e32 v19, v130, v4
	v_fmac_f32_e32 v19, v131, v5
	v_add_f32_e32 v24, v24, v19
	s_waitcnt vmcnt(2)
	v_mul_f32_e32 v19, v133, v7
	v_fmac_f32_e32 v19, v132, v6
	v_fmac_f32_e32 v19, v134, v8
	v_fmac_f32_e32 v19, v135, v9
	v_add_f32_e32 v24, v24, v19
	s_waitcnt vmcnt(1)
	v_mul_f32_e32 v19, v137, v15
	v_fmac_f32_e32 v19, v136, v14
	v_fmac_f32_e32 v19, v138, v16
	v_fmac_f32_e32 v19, v139, v17
	v_add_f32_e32 v18, v24, v19
	v_mov_b32_e32 v19, 0
	s_nop 0
	v_add_f32_dpp v18, v18, v18 quad_perm:[1,0,3,2] row_mask:0xf bank_mask:0xf bound_ctrl:1
	s_nop 1
	v_add_f32_dpp v18, v18, v18 quad_perm:[2,3,0,1] row_mask:0xf bank_mask:0xf bound_ctrl:1
	s_nop 1
	v_add_f32_dpp v18, v18, v18 row_half_mirror row_mask:0xf bank_mask:0xf bound_ctrl:1
	s_nop 1
	v_add_f32_dpp v18, v18, v18 row_mirror row_mask:0xf bank_mask:0xf bound_ctrl:1
	s_nop 1
	v_mov_b32_dpp v19, v18 row_bcast:15 row_mask:0xa bank_mask:0xf
	v_add_f32_e32 v18, v18, v19
	v_mov_b32_e32 v19, 0
	s_nop 1
	v_mov_b32_dpp v19, v18 row_bcast:31 row_mask:0xc bank_mask:0xf
	v_add_f32_e32 v18, v18, v19
	s_nop 0
	v_readlane_b32 s1, v18, 63
	s_and_saveexec_b64 s[24:25], s[40:41]
	s_cbranch_execz .LBB0_1206
	v_mov_b32_e32 v19, s27
	s_waitcnt vmcnt(0)
	v_add_f32_e32 v18, s1, v140
	ds_write_b32 v19, v18
	s_branch .LBB0_1206
